# weight-conversion split 80/20 between the w_in phase and the router phase (one more point on the split curve; 85/15 was the previous version)
# baseline (speedup 1.0000x reference)
; DI CvItem cv_decode(const Params& P, int it) { CvItem c; int item;
;     if (it < NE * CV_GU1) { const int e = it / CV_GU1; c.W = P.in[I_WGU] + (size_t)e * D * 4096; c.N = 4096; c.WT = (unsigned char*)(P.ws + WS_WGU) + (size_t)e * 4096 * D; c.kind = 2; item = it % CV_GU1; }
;     else { const int r = it - NE * CV_GU1; const int e = r / CV_DN1; c.W = P.in[I_WDN] + (size_t)e * D * D; c.N = D; c.WT = (unsigned char*)(P.ws + WS_WDN) + (size_t)e * D * D; c.kind = 3; item = r % CV_DN1; }
;     const int nblk = c.N / 32, kb = item / nblk, nb = item % nblk; c.k0 = 128 * kb; c.n0 = 32 * nb; return c; }
; DI void conv_pool(const Params& P, LAS unsigned char* lds, int pool, int blk_lo, int blk_hi) {
;     ...
;     auto claim = [&]() -> int { unsigned v_ = 0u; if (lane == 0) v_ = __hip_atomic_fetch_add(ctr, 1u, __ATOMIC_RELAXED, __HIP_MEMORY_SCOPE_AGENT); return blk_lo + (int)__builtin_amdgcn_readfirstlane(v_); };
;     const int blk = claim(); if (blk >= CV_NBLK) return;
;     int it = blk * CV_BLK, left = CV_BLK;
;     CvItem cur = cv_decode(P, it); f32x4 v[16]; cv_issue(cur, lane, v);
.LBB0_363:
	s_or_b64 exec, exec, s[2:3]
	v_readfirstlane_b32 s13, v0
	s_cmpk_gt_i32 s13, 0x2665
	s_cbranch_scc1 .LBB0_383
	s_lshl_b32 s38, s13, 3
	s_cmpk_gt_i32 s13, 0x1fff
	s_mov_b32 s11, 3
	s_cbranch_scc0 .LBB0_366
	s_add_i32 s2, s38, 0xffff0000
	s_lshr_b32 s2, s2, 10
	s_mov_b32 s3, 0
	v_readlane_b32 s48, v254, 6
	s_lshl_b64 s[6:7], s[2:3], 22
	s_lshl_b64 s[2:3], s[2:3], 24
	v_readlane_b32 s50, v254, 8
	v_readlane_b32 s51, v254, 9
	s_add_u32 s14, s50, s2
	v_readlane_b32 s40, v254, 2
	s_addc_u32 s15, s51, s3
	v_readlane_b32 s42, v254, 4
	v_readlane_b32 s43, v254, 5
	s_add_u32 s2, s42, s6
	s_addc_u32 s3, s43, s7
	s_add_u32 s6, s2, 0x12400000
	v_readlane_b32 s49, v254, 7
	v_readlane_b32 s52, v254, 10
	v_readlane_b32 s53, v254, 11
	v_readlane_b32 s54, v254, 12
	v_readlane_b32 s55, v254, 13
	v_readlane_b32 s41, v254, 3
	s_addc_u32 s7, s3, 0
	s_and_b32 s10, s38, 0x3f8
	s_movk_i32 s16, 0x800
	s_cbranch_execz .LBB0_367
	s_branch .LBB0_368

; DI void conv_pool(const Params& P, LAS unsigned char* lds, int pool, int blk_lo, int blk_hi) {
;     ...
;     for (;;) { int nx = it + 1; bool more = true;
;     ...
;         const CvItem nxt = cv_decode(P, nx); f32x4 vn[16]; cv_issue(nxt, lane, vn);
.LBB0_376:
	s_or_b64 exec, exec, s[2:3]
	v_readfirstlane_b32 s2, v56
	s_lshl_b32 s22, s2, 3
	s_cmpk_lt_i32 s2, 0x2666
	s_cselect_b64 s[2:3], -1, 0
	s_and_b64 s[16:17], s[2:3], exec
	s_cselect_b32 s43, 8, s14
	s_cselect_b32 s44, s22, s38
	s_branch .LBB0_379

; DI CvItem cv_decode(const Params& P, int it) { CvItem c; int item;
;     if (it < NE * CV_GU1) { const int e = it / CV_GU1; c.W = P.in[I_WGU] + (size_t)e * D * 4096; c.N = 4096; c.WT = (unsigned char*)(P.ws + WS_WGU) + (size_t)e * 4096 * D; c.kind = 2; item = it % CV_GU1; }
;     else { const int r = it - NE * CV_GU1; const int e = r / CV_DN1; c.W = P.in[I_WDN] + (size_t)e * D * D; c.N = D; c.WT = (unsigned char*)(P.ws + WS_WDN) + (size_t)e * D * D; c.kind = 3; item = r % CV_DN1; }
;     const int nblk = c.N / 32, kb = item / nblk, nb = item % nblk; c.k0 = 128 * kb; c.n0 = 32 * nb; return c; }
; DI void conv_pool(const Params& P, LAS unsigned char* lds, int pool, int blk_lo, int blk_hi) {
;     ...
;     auto claim = [&]() -> int { unsigned v_ = 0u; if (lane == 0) v_ = __hip_atomic_fetch_add(ctr, 1u, __ATOMIC_RELAXED, __HIP_MEMORY_SCOPE_AGENT); return blk_lo + (int)__builtin_amdgcn_readfirstlane(v_); };
;     const int blk = claim(); if (blk >= CV_NBLK) return;
;     int it = blk * CV_BLK, left = CV_BLK;
;     CvItem cur = cv_decode(P, it); f32x4 v[16]; cv_issue(cur, lane, v);
.LBB0_1116:
	s_or_b64 exec, exec, s[2:3]
	v_readfirstlane_b32 s2, v0
	s_cmpk_gt_i32 s2, 0x999
	s_cbranch_scc1 .LBB0_1136
	s_add_i32 s13, s2, 0x2666
	s_lshl_b32 s20, s13, 3
	s_cmpk_gt_i32 s2, 0xf999
	s_mov_b32 s11, 3
	s_cbranch_scc0 .LBB0_1119
	s_add_i32 s2, s20, 0xffff0000
	v_readlane_b32 s36, v254, 6
	s_lshr_b32 s2, s2, 10
	s_mov_b32 s3, 0
	v_readlane_b32 s38, v254, 8
	v_readlane_b32 s39, v254, 9
	s_lshl_b64 s[6:7], s[2:3], 22
	s_lshl_b64 s[2:3], s[2:3], 24
	s_mov_b64 s[14:15], s[38:39]
	s_add_u32 s14, s14, s2
	v_readlane_b32 s16, v254, 2
	s_addc_u32 s15, s15, s3
	v_readlane_b32 s18, v254, 4
	v_readlane_b32 s19, v254, 5
	s_add_u32 s2, s18, s6
	s_addc_u32 s3, s19, s7
	s_add_u32 s6, s2, 0x12400000
	v_readlane_b32 s37, v254, 7
	v_readlane_b32 s40, v254, 10
	v_readlane_b32 s41, v254, 11
	v_readlane_b32 s42, v254, 12
	v_readlane_b32 s43, v254, 13
	v_readlane_b32 s17, v254, 3
	s_addc_u32 s7, s3, 0
	s_and_b32 s10, s20, 0x3f8
	s_movk_i32 s16, 0x800
	s_cbranch_execz .LBB0_1120
	s_branch .LBB0_1121

; DI void conv_pool(const Params& P, LAS unsigned char* lds, int pool, int blk_lo, int blk_hi) {
;     ...
;     for (;;) { int nx = it + 1; bool more = true;
;     ...
;         const CvItem nxt = cv_decode(P, nx); f32x4 vn[16]; cv_issue(nxt, lane, vn);
.LBB0_1129:
	s_or_b64 exec, exec, s[2:3]
	v_readfirstlane_b32 s2, v56
	s_lshl_b32 s3, s2, 3
	s_add_i32 s18, s3, 0x13330
	s_cmpk_lt_i32 s2, 0x99a
	s_cselect_b64 s[2:3], -1, 0
	s_and_b64 s[16:17], s[2:3], exec
	s_cselect_b32 s28, 8, s14
	s_cselect_b32 s29, s18, s20
	s_branch .LBB0_1132
